# peel first K-iteration of the 4 GEMM unit loops (C=0, no accumulator zeroing) + hoist V LDS-DMA issue before first MFMA group in attention + pk-split softmax
# speedup vs baseline: 1.0101x; 1.0101x over previous
.LBB0_191:
	s_ashr_i32 s61, s60, 31
	s_lshl_b64 s[62:63], s[60:61], 19
	s_add_u32 s62, s12, s62
	s_addc_u32 s63, s13, s63
	s_ashr_i32 s59, s58, 31
	s_lshl_b64 s[64:65], s[58:59], 19
	s_add_u32 s64, s14, s64
	s_addc_u32 s65, s15, s65
	s_andn2_b64 vcc, exec, s[30:31]
	s_cbranch_vccnz .LBB0_195
	v_cmp_lt_i64_e32 vcc, s[68:69], v[142:143]
	s_and_b64 s[68:69], vcc, exec
	s_cselect_b32 s9, s63, s11
	s_cselect_b32 s59, s62, s10
	s_cselect_b32 s61, s65, s67
	s_cselect_b32 s86, s64, s66
	s_add_u32 s10, s10, 0x40080
	s_addc_u32 s11, s11, 0
	s_add_u32 s87, s66, 0x100
	s_addc_u32 s88, s67, 0
	s_mov_b32 s66, 0
	s_waitcnt vmcnt(0)
	v_add_u32_e32 v154, s77, v157
	ds_read_b128 v[146:149], v154
	ds_read_b128 v[150:153], v154 offset:1024
	ds_read_b128 v[164:167], v154 offset:2048
	ds_read_b128 v[168:171], v154 offset:3072
	s_add_i32 s89, s66, 2
	s_add_u32 s67, s10, 0xfffc0080
	s_addc_u32 s68, s11, -1
	s_cmp_eq_u32 s75, s66
	s_cselect_b32 s66, s86, s87
	s_cselect_b32 s69, s9, s68
	s_cselect_b32 s68, s59, s67
	s_cselect_b32 s67, s61, s88
	v_lshl_add_u64 v[206:207], s[10:11], 0, v[138:139]
	s_add_i32 m0, s52, 0xc000
	ds_read_b128 v[172:175], v159
	ds_read_b128 v[176:179], v159 offset:1024
	ds_read_b128 v[180:183], v159 offset:2048
	ds_read_b128 v[184:187], v159 offset:3072
	ds_read_b128 v[188:191], v159 offset:4096
	ds_read_b128 v[192:195], v159 offset:5120
	ds_read_b128 v[198:201], v159 offset:6144
	ds_read_b128 v[202:205], v159 offset:7168
	global_load_lds_dwordx4 v[206:207], off
	v_lshl_add_u64 v[206:207], s[10:11], 0, v[140:141]
	s_add_i32 m0, s52, 0xe000
	s_nop 0
	global_load_lds_dwordx4 v[206:207], off
	s_waitcnt lgkmcnt(8)
	s_barrier
	s_waitcnt lgkmcnt(0)
	s_setprio 1
	s_waitcnt lgkmcnt(0)
	v_mfma_i32_16x16x64_i8 v[62:65], v[146:149], v[172:175], 0
	v_mfma_i32_16x16x64_i8 v[58:61], v[164:167], v[172:175], 0
	v_mfma_i32_16x16x64_i8 v[54:57], v[146:149], v[180:183], 0
	v_mfma_i32_16x16x64_i8 v[50:53], v[164:167], v[180:183], 0
	v_mfma_i32_16x16x64_i8 v[46:49], v[146:149], v[188:191], 0
	v_mfma_i32_16x16x64_i8 v[42:45], v[164:167], v[188:191], 0
	v_mfma_i32_16x16x64_i8 v[38:41], v[146:149], v[198:201], 0
	v_mfma_i32_16x16x64_i8 v[34:37], v[164:167], v[198:201], 0
	v_mfma_i32_16x16x64_i8 v[62:65], v[150:153], v[176:179], v[62:65]
	v_mfma_i32_16x16x64_i8 v[58:61], v[168:171], v[176:179], v[58:61]
	v_mfma_i32_16x16x64_i8 v[54:57], v[150:153], v[184:187], v[54:57]
	v_mfma_i32_16x16x64_i8 v[50:53], v[168:171], v[184:187], v[50:53]
	v_mfma_i32_16x16x64_i8 v[46:49], v[150:153], v[192:195], v[46:49]
	v_mfma_i32_16x16x64_i8 v[42:45], v[168:171], v[192:195], v[42:45]
	v_mfma_i32_16x16x64_i8 v[38:41], v[150:153], v[202:205], v[38:41]
	v_mfma_i32_16x16x64_i8 v[34:37], v[168:171], v[202:205], v[34:37]
	s_setprio 0
	s_barrier
	s_add_i32 s90, s77, s4
	v_add_u32_e32 v154, s78, v157
	v_lshl_add_u64 v[222:223], s[66:67], 0, v[134:135]
	s_mov_b32 m0, s90
	ds_read_b128 v[206:209], v154
	ds_read_b128 v[210:213], v154 offset:1024
	ds_read_b128 v[214:217], v154 offset:2048
	ds_read_b128 v[218:221], v154 offset:3072
	global_load_lds_dwordx4 v[222:223], off
	v_lshl_add_u64 v[224:225], s[66:67], 0, v[130:131]
	s_add_i32 m0, s90, 0x2000
	s_nop 0
	global_load_lds_dwordx4 v[224:225], off
	s_barrier
	s_waitcnt lgkmcnt(0)
	s_setprio 1
	s_waitcnt lgkmcnt(0)
	v_mfma_i32_16x16x64_i8 v[126:129], v[206:209], v[172:175], 0
	v_mfma_i32_16x16x64_i8 v[122:125], v[214:217], v[172:175], 0
	v_mfma_i32_16x16x64_i8 v[118:121], v[206:209], v[180:183], 0
	v_mfma_i32_16x16x64_i8 v[114:117], v[214:217], v[180:183], 0
	v_mfma_i32_16x16x64_i8 v[110:113], v[206:209], v[188:191], 0
	v_mfma_i32_16x16x64_i8 v[106:109], v[214:217], v[188:191], 0
	v_mfma_i32_16x16x64_i8 v[102:105], v[206:209], v[198:201], 0
	v_mfma_i32_16x16x64_i8 v[98:101], v[214:217], v[198:201], 0
	v_mfma_i32_16x16x64_i8 v[126:129], v[210:213], v[176:179], v[126:129]
	v_mfma_i32_16x16x64_i8 v[122:125], v[218:221], v[176:179], v[122:125]
	v_mfma_i32_16x16x64_i8 v[118:121], v[210:213], v[184:187], v[118:121]
	v_mfma_i32_16x16x64_i8 v[114:117], v[218:221], v[184:187], v[114:117]
	v_mfma_i32_16x16x64_i8 v[110:113], v[210:213], v[192:195], v[110:113]
	v_mfma_i32_16x16x64_i8 v[106:109], v[218:221], v[192:195], v[106:109]
	v_mfma_i32_16x16x64_i8 v[102:105], v[210:213], v[202:205], v[102:105]
	v_mfma_i32_16x16x64_i8 v[98:101], v[218:221], v[202:205], v[98:101]
	s_setprio 0
	s_mov_b32 m0, s52
	v_lshl_add_u64 v[226:227], s[68:69], 0, v[136:137]
	s_barrier
	ds_read_b128 v[172:175], v159 offset:16384
	ds_read_b128 v[176:179], v159 offset:17408
	ds_read_b128 v[180:183], v159 offset:18432
	ds_read_b128 v[184:187], v159 offset:19456
	ds_read_b128 v[188:191], v159 offset:20480
	ds_read_b128 v[192:195], v159 offset:21504
	ds_read_b128 v[198:201], v159 offset:22528
	ds_read_b128 v[202:205], v159 offset:23552
	global_load_lds_dwordx4 v[226:227], off
	v_lshl_add_u64 v[228:229], s[68:69], 0, v[132:133]
	s_mov_b32 m0, s53
	s_nop 0
	global_load_lds_dwordx4 v[228:229], off
	s_barrier
	s_waitcnt lgkmcnt(0)
	s_setprio 1
	s_waitcnt lgkmcnt(0)
	v_mfma_i32_16x16x64_i8 v[30:33], v[146:149], v[172:175], 0
	v_mfma_i32_16x16x64_i8 v[26:29], v[164:167], v[172:175], 0
	v_mfma_i32_16x16x64_i8 v[22:25], v[146:149], v[180:183], 0
	v_mfma_i32_16x16x64_i8 v[18:21], v[164:167], v[180:183], 0
	v_mfma_i32_16x16x64_i8 v[14:17], v[146:149], v[188:191], 0
	v_mfma_i32_16x16x64_i8 v[10:13], v[164:167], v[188:191], 0
	v_mfma_i32_16x16x64_i8 v[6:9], v[146:149], v[198:201], 0
	v_mfma_i32_16x16x64_i8 v[2:5], v[164:167], v[198:201], 0
	v_mfma_i32_16x16x64_i8 v[30:33], v[150:153], v[176:179], v[30:33]
	v_mfma_i32_16x16x64_i8 v[26:29], v[168:171], v[176:179], v[26:29]
	v_mfma_i32_16x16x64_i8 v[22:25], v[150:153], v[184:187], v[22:25]
	v_mfma_i32_16x16x64_i8 v[18:21], v[168:171], v[184:187], v[18:21]
	v_mfma_i32_16x16x64_i8 v[14:17], v[150:153], v[192:195], v[14:17]
	v_mfma_i32_16x16x64_i8 v[10:13], v[168:171], v[192:195], v[10:13]
	v_mfma_i32_16x16x64_i8 v[6:9], v[150:153], v[202:205], v[6:9]
	v_mfma_i32_16x16x64_i8 v[2:5], v[168:171], v[202:205], v[2:5]
	s_setprio 0
	s_barrier
	s_add_u32 s90, s66, 0x40000
	s_addc_u32 s91, s67, 0
	s_add_i32 s92, s78, s4
	v_lshl_add_u64 v[146:147], s[90:91], 0, v[134:135]
	s_mov_b32 m0, s92
	s_nop 0
	global_load_lds_dwordx4 v[146:147], off
	v_lshl_add_u64 v[146:147], s[90:91], 0, v[130:131]
	s_add_i32 m0, s92, 0x2000
	s_nop 0
	global_load_lds_dwordx4 v[146:147], off
	s_waitcnt vmcnt(6)
	s_barrier
	s_setprio 1
	v_mfma_i32_16x16x64_i8 v[94:97], v[206:209], v[172:175], 0
	v_mfma_i32_16x16x64_i8 v[90:93], v[214:217], v[172:175], 0
	v_mfma_i32_16x16x64_i8 v[86:89], v[206:209], v[180:183], 0
	v_mfma_i32_16x16x64_i8 v[82:85], v[214:217], v[180:183], 0
	v_mfma_i32_16x16x64_i8 v[78:81], v[206:209], v[188:191], 0
	v_mfma_i32_16x16x64_i8 v[74:77], v[214:217], v[188:191], 0
	v_mfma_i32_16x16x64_i8 v[70:73], v[206:209], v[198:201], 0
	v_mfma_i32_16x16x64_i8 v[66:69], v[214:217], v[198:201], 0
	v_mfma_i32_16x16x64_i8 v[94:97], v[210:213], v[176:179], v[94:97]
	v_mfma_i32_16x16x64_i8 v[90:93], v[218:221], v[176:179], v[90:93]
	v_mfma_i32_16x16x64_i8 v[86:89], v[210:213], v[184:187], v[86:89]
	v_mfma_i32_16x16x64_i8 v[82:85], v[218:221], v[184:187], v[82:85]
	v_mfma_i32_16x16x64_i8 v[78:81], v[210:213], v[192:195], v[78:81]
	v_mfma_i32_16x16x64_i8 v[74:77], v[218:221], v[192:195], v[74:77]
	v_mfma_i32_16x16x64_i8 v[70:73], v[210:213], v[202:205], v[70:73]
	v_mfma_i32_16x16x64_i8 v[66:69], v[218:221], v[202:205], v[66:69]
	s_setprio 0
	s_add_i32 s90, 0, 0x18000
	v_add_u32_e32 v154, s90, v157
	s_barrier
	ds_read_b128 v[146:149], v154
	ds_read_b128 v[150:153], v154 offset:1024
	ds_read_b128 v[164:167], v154 offset:2048
	ds_read_b128 v[168:171], v154 offset:3072
	s_add_u32 s68, s68, 0x40000
	s_addc_u32 s69, s69, 0
	s_mov_b32 m0, s54
	v_lshl_add_u64 v[206:207], s[68:69], 0, v[136:137]
	ds_read_b128 v[172:175], v159 offset:32768
	ds_read_b128 v[176:179], v159 offset:33792
	ds_read_b128 v[180:183], v159 offset:34816
	ds_read_b128 v[184:187], v159 offset:35840
	ds_read_b128 v[188:191], v159 offset:36864
	ds_read_b128 v[192:195], v159 offset:37888
	ds_read_b128 v[198:201], v159 offset:38912
	ds_read_b128 v[202:205], v159 offset:39936
	global_load_lds_dwordx4 v[206:207], off
	v_lshl_add_u64 v[206:207], s[68:69], 0, v[132:133]
	s_mov_b32 m0, s55
	s_nop 0
	global_load_lds_dwordx4 v[206:207], off
	s_waitcnt lgkmcnt(8)
	s_barrier
	s_waitcnt lgkmcnt(0)
	s_setprio 1
	s_waitcnt lgkmcnt(0)
	v_mfma_i32_16x16x64_i8 v[62:65], v[146:149], v[172:175], v[62:65]
	v_mfma_i32_16x16x64_i8 v[58:61], v[164:167], v[172:175], v[58:61]
	v_mfma_i32_16x16x64_i8 v[54:57], v[146:149], v[180:183], v[54:57]
	v_mfma_i32_16x16x64_i8 v[50:53], v[164:167], v[180:183], v[50:53]
	v_mfma_i32_16x16x64_i8 v[46:49], v[146:149], v[188:191], v[46:49]
	v_mfma_i32_16x16x64_i8 v[42:45], v[164:167], v[188:191], v[42:45]
	v_mfma_i32_16x16x64_i8 v[38:41], v[146:149], v[198:201], v[38:41]
	v_mfma_i32_16x16x64_i8 v[34:37], v[164:167], v[198:201], v[34:37]
	v_mfma_i32_16x16x64_i8 v[62:65], v[150:153], v[176:179], v[62:65]
	v_mfma_i32_16x16x64_i8 v[58:61], v[168:171], v[176:179], v[58:61]
	v_mfma_i32_16x16x64_i8 v[54:57], v[150:153], v[184:187], v[54:57]
	v_mfma_i32_16x16x64_i8 v[50:53], v[168:171], v[184:187], v[50:53]
	v_mfma_i32_16x16x64_i8 v[46:49], v[150:153], v[192:195], v[46:49]
	v_mfma_i32_16x16x64_i8 v[42:45], v[168:171], v[192:195], v[42:45]
	v_mfma_i32_16x16x64_i8 v[38:41], v[150:153], v[202:205], v[38:41]
	v_mfma_i32_16x16x64_i8 v[34:37], v[168:171], v[202:205], v[34:37]
	s_setprio 0
	s_barrier
	s_add_i32 s68, 0, 0x1c000
	s_add_i32 s69, s90, s4
	v_add_u32_e32 v154, s68, v157
	v_lshl_add_u64 v[222:223], v[222:223], 0, s[28:29]
	s_mov_b32 m0, s69
	ds_read_b128 v[206:209], v154
	ds_read_b128 v[210:213], v154 offset:1024
	ds_read_b128 v[214:217], v154 offset:2048
	ds_read_b128 v[218:221], v154 offset:3072
	global_load_lds_dwordx4 v[222:223], off
	v_lshl_add_u64 v[222:223], v[224:225], 0, s[28:29]
	s_add_i32 m0, s69, 0x2000
	s_nop 0
	global_load_lds_dwordx4 v[222:223], off
	s_barrier
	s_waitcnt lgkmcnt(0)
	s_setprio 1
	s_waitcnt lgkmcnt(0)
	v_mfma_i32_16x16x64_i8 v[126:129], v[206:209], v[172:175], v[126:129]
	v_mfma_i32_16x16x64_i8 v[122:125], v[214:217], v[172:175], v[122:125]
	v_mfma_i32_16x16x64_i8 v[118:121], v[206:209], v[180:183], v[118:121]
	v_mfma_i32_16x16x64_i8 v[114:117], v[214:217], v[180:183], v[114:117]
	v_mfma_i32_16x16x64_i8 v[110:113], v[206:209], v[188:191], v[110:113]
	v_mfma_i32_16x16x64_i8 v[106:109], v[214:217], v[188:191], v[106:109]
	v_mfma_i32_16x16x64_i8 v[102:105], v[206:209], v[198:201], v[102:105]
	v_mfma_i32_16x16x64_i8 v[98:101], v[214:217], v[198:201], v[98:101]
	v_mfma_i32_16x16x64_i8 v[126:129], v[210:213], v[176:179], v[126:129]
	v_mfma_i32_16x16x64_i8 v[122:125], v[218:221], v[176:179], v[122:125]
	v_mfma_i32_16x16x64_i8 v[118:121], v[210:213], v[184:187], v[118:121]
	v_mfma_i32_16x16x64_i8 v[114:117], v[218:221], v[184:187], v[114:117]
	v_mfma_i32_16x16x64_i8 v[110:113], v[210:213], v[192:195], v[110:113]
	v_mfma_i32_16x16x64_i8 v[106:109], v[218:221], v[192:195], v[106:109]
	v_mfma_i32_16x16x64_i8 v[102:105], v[210:213], v[202:205], v[102:105]
	v_mfma_i32_16x16x64_i8 v[98:101], v[218:221], v[202:205], v[98:101]
	s_setprio 0
	s_mov_b32 m0, s73
	v_lshl_add_u64 v[222:223], v[226:227], 0, s[28:29]
	s_barrier
	ds_read_b128 v[172:175], v159 offset:49152
	ds_read_b128 v[176:179], v159 offset:50176
	ds_read_b128 v[180:183], v159 offset:51200
	ds_read_b128 v[184:187], v159 offset:52224
	ds_read_b128 v[188:191], v159 offset:53248
	ds_read_b128 v[192:195], v159 offset:54272
	ds_read_b128 v[198:201], v159 offset:55296
	ds_read_b128 v[202:205], v159 offset:56320
	global_load_lds_dwordx4 v[222:223], off
	v_lshl_add_u64 v[222:223], v[228:229], 0, s[28:29]
	s_mov_b32 m0, s74
	s_nop 0
	global_load_lds_dwordx4 v[222:223], off
	s_barrier
	s_waitcnt lgkmcnt(0)
	s_setprio 1
	s_waitcnt lgkmcnt(0)
	v_mfma_i32_16x16x64_i8 v[30:33], v[146:149], v[172:175], v[30:33]
	v_mfma_i32_16x16x64_i8 v[26:29], v[164:167], v[172:175], v[26:29]
	v_mfma_i32_16x16x64_i8 v[22:25], v[146:149], v[180:183], v[22:25]
	v_mfma_i32_16x16x64_i8 v[18:21], v[164:167], v[180:183], v[18:21]
	v_mfma_i32_16x16x64_i8 v[14:17], v[146:149], v[188:191], v[14:17]
	v_mfma_i32_16x16x64_i8 v[10:13], v[164:167], v[188:191], v[10:13]
	v_mfma_i32_16x16x64_i8 v[6:9], v[146:149], v[198:201], v[6:9]
	v_mfma_i32_16x16x64_i8 v[2:5], v[164:167], v[198:201], v[2:5]
	v_mfma_i32_16x16x64_i8 v[30:33], v[150:153], v[176:179], v[30:33]
	v_mfma_i32_16x16x64_i8 v[26:29], v[168:171], v[176:179], v[26:29]
	v_mfma_i32_16x16x64_i8 v[22:25], v[150:153], v[184:187], v[22:25]
	v_mfma_i32_16x16x64_i8 v[18:21], v[168:171], v[184:187], v[18:21]
	v_mfma_i32_16x16x64_i8 v[14:17], v[150:153], v[192:195], v[14:17]
	v_mfma_i32_16x16x64_i8 v[10:13], v[168:171], v[192:195], v[10:13]
	v_mfma_i32_16x16x64_i8 v[6:9], v[150:153], v[202:205], v[6:9]
	v_mfma_i32_16x16x64_i8 v[2:5], v[168:171], v[202:205], v[2:5]
	s_setprio 0
	s_barrier
	s_add_u32 s66, s66, 0x40080
	s_addc_u32 s67, s67, 0
	s_add_i32 s68, s68, s4
	v_lshl_add_u64 v[146:147], s[66:67], 0, v[134:135]
	s_mov_b32 m0, s68
	s_nop 0
	global_load_lds_dwordx4 v[146:147], off
	v_lshl_add_u64 v[146:147], s[66:67], 0, v[130:131]
	s_add_i32 m0, s68, 0x2000
	s_nop 0
	global_load_lds_dwordx4 v[146:147], off
	s_waitcnt vmcnt(6)
	s_barrier
	s_setprio 1
	v_mfma_i32_16x16x64_i8 v[94:97], v[206:209], v[172:175], v[94:97]
	v_mfma_i32_16x16x64_i8 v[90:93], v[214:217], v[172:175], v[90:93]
	v_mfma_i32_16x16x64_i8 v[86:89], v[206:209], v[180:183], v[86:89]
	v_mfma_i32_16x16x64_i8 v[82:85], v[214:217], v[180:183], v[82:85]
	v_mfma_i32_16x16x64_i8 v[78:81], v[206:209], v[188:191], v[78:81]
	v_mfma_i32_16x16x64_i8 v[74:77], v[214:217], v[188:191], v[74:77]
	v_mfma_i32_16x16x64_i8 v[70:73], v[206:209], v[198:201], v[70:73]
	v_mfma_i32_16x16x64_i8 v[66:69], v[214:217], v[198:201], v[66:69]
	v_mfma_i32_16x16x64_i8 v[94:97], v[210:213], v[176:179], v[94:97]
	v_mfma_i32_16x16x64_i8 v[90:93], v[218:221], v[176:179], v[90:93]
	v_mfma_i32_16x16x64_i8 v[86:89], v[210:213], v[184:187], v[86:89]
	v_mfma_i32_16x16x64_i8 v[82:85], v[218:221], v[184:187], v[82:85]
	v_mfma_i32_16x16x64_i8 v[78:81], v[210:213], v[192:195], v[78:81]
	v_mfma_i32_16x16x64_i8 v[74:77], v[218:221], v[192:195], v[74:77]
	v_mfma_i32_16x16x64_i8 v[70:73], v[210:213], v[202:205], v[70:73]
	v_mfma_i32_16x16x64_i8 v[66:69], v[218:221], v[202:205], v[66:69]
	s_setprio 0
	s_add_u32 s10, s10, 0x100
	s_addc_u32 s11, s11, 0
	s_add_u32 s87, s87, 0x100
	s_addc_u32 s88, s88, 0
	s_cmp_ge_i32 s89, s1
	s_mov_b32 s66, s89
	s_barrier
	s_cbranch_scc0 .LBB0_193
	s_branch .Lmy_pl0_exit

.Lmy_pl0_exit:
	v_cvt_f32_i32_e32 v150, v126
	v_cvt_f32_i32_e32 v151, v127
	v_cvt_f32_i32_e32 v126, v128
	v_cvt_f32_i32_e32 v127, v129
	v_cvt_f32_i32_e32 v148, v122
	v_cvt_f32_i32_e32 v149, v123
	v_cvt_f32_i32_e32 v152, v124
	v_cvt_f32_i32_e32 v153, v125
	v_cvt_f32_i32_e32 v124, v118
	v_cvt_f32_i32_e32 v125, v119
	v_cvt_f32_i32_e32 v146, v120
	v_cvt_f32_i32_e32 v147, v121
	v_cvt_f32_i32_e32 v122, v114
	v_cvt_f32_i32_e32 v123, v115
	v_cvt_f32_i32_e32 v128, v116
	v_cvt_f32_i32_e32 v129, v117
	v_cvt_f32_i32_e32 v114, v110
	v_cvt_f32_i32_e32 v115, v111
	v_cvt_f32_i32_e32 v120, v112
	v_cvt_f32_i32_e32 v121, v113
	v_cvt_f32_i32_e32 v110, v106
	v_cvt_f32_i32_e32 v111, v107
	v_cvt_f32_i32_e32 v118, v108
	v_cvt_f32_i32_e32 v119, v109
	v_cvt_f32_i32_e32 v102, v102
	v_cvt_f32_i32_e32 v103, v103
	v_cvt_f32_i32_e32 v104, v104
	v_cvt_f32_i32_e32 v105, v105
	v_cvt_f32_i32_e32 v98, v98
	v_cvt_f32_i32_e32 v99, v99
	v_cvt_f32_i32_e32 v100, v100
	v_cvt_f32_i32_e32 v101, v101
	v_cvt_f32_i32_e32 v108, v94
	v_cvt_f32_i32_e32 v109, v95
	v_cvt_f32_i32_e32 v116, v96
	v_cvt_f32_i32_e32 v117, v97
	v_cvt_f32_i32_e32 v106, v90
	v_cvt_f32_i32_e32 v107, v91
	v_cvt_f32_i32_e32 v112, v92
	v_cvt_f32_i32_e32 v113, v93
	v_cvt_f32_i32_e32 v92, v86
	v_cvt_f32_i32_e32 v93, v87
	v_cvt_f32_i32_e32 v96, v88
	v_cvt_f32_i32_e32 v97, v89
	v_cvt_f32_i32_e32 v90, v82
	v_cvt_f32_i32_e32 v91, v83
	v_cvt_f32_i32_e32 v94, v84
	v_cvt_f32_i32_e32 v95, v85
	v_cvt_f32_i32_e32 v84, v78
	v_cvt_f32_i32_e32 v85, v79
	v_cvt_f32_i32_e32 v88, v80
	v_cvt_f32_i32_e32 v89, v81
	v_cvt_f32_i32_e32 v82, v74
	v_cvt_f32_i32_e32 v83, v75
	v_cvt_f32_i32_e32 v86, v76
	v_cvt_f32_i32_e32 v87, v77
	v_cvt_f32_i32_e32 v76, v70
	v_cvt_f32_i32_e32 v77, v71
	v_cvt_f32_i32_e32 v80, v72
	v_cvt_f32_i32_e32 v81, v73
	v_cvt_f32_i32_e32 v74, v66
	v_cvt_f32_i32_e32 v75, v67
	v_cvt_f32_i32_e32 v78, v68
	v_cvt_f32_i32_e32 v79, v69
	s_branch .LBB0_196

.LBB0_534:
	s_add_i32 s44, s38, 1
	s_cmp_ge_i32 s44, s35
	s_cbranch_scc1 .Lmy_vdma_skip
	v_lshl_add_u64 v[16:17], s[94:95], 0, v[206:207]
	s_mov_b64 s[46:47], 0x162400
	s_add_i32 s45, s34, s10
	v_lshl_add_u64 v[236:237], v[16:17], 0, s[46:47]
	s_mov_b32 m0, s45
	s_mov_b64 s[10:11], 0x162480
	global_load_lds_dwordx4 v[236:237], off
	v_lshl_add_u64 v[16:17], v[16:17], 0, s[10:11]
	s_add_i32 m0, s45, 0x400
	s_nop 0
	global_load_lds_dwordx4 v[16:17], off
.Lmy_vdma_skip:
	s_waitcnt lgkmcnt(8)
	v_mfma_f32_32x32x16_bf16 v[82:97], v[146:149], v[110:113], v[82:97]
	v_mfma_f32_32x32x16_bf16 v[82:97], v[150:153], v[106:109], v[82:97]
	v_mfma_f32_32x32x16_bf16 v[82:97], v[154:157], v[102:105], v[82:97]
	v_mfma_f32_32x32x16_bf16 v[82:97], v[158:161], v[98:101], v[82:97]
	ds_read_b64_tr_b16 v[194:195], v2 offset:0x200
	ds_read_b64_tr_b16 v[196:197], v2 offset:0xa00
	ds_read_b64_tr_b16 v[190:191], v2 offset:0x1200
	ds_read_b64_tr_b16 v[192:193], v2 offset:0x1a00
	ds_read_b64_tr_b16 v[186:187], v2 offset:0x2200
	ds_read_b64_tr_b16 v[188:189], v2 offset:0x2a00
	ds_read_b64_tr_b16 v[182:183], v2 offset:0x3200
	ds_read_b64_tr_b16 v[184:185], v2 offset:0x3a00
.LBB0_536:
	s_waitcnt lgkmcnt(8)
	v_mfma_f32_32x32x16_bf16 v[114:129], v[4:7], v[130:133], v[18:33]
	v_mfma_f32_32x32x16_bf16 v[98:113], v[8:11], v[130:133], v[18:33]
	v_mfma_f32_32x32x16_bf16 v[114:129], v[170:173], v[134:137], v[114:129]
	v_mfma_f32_32x32x16_bf16 v[98:113], v[12:15], v[134:137], v[98:113]
	v_mfma_f32_32x32x16_bf16 v[114:129], v[174:177], v[138:141], v[114:129]
	v_mfma_f32_32x32x16_bf16 v[98:113], v[162:165], v[138:141], v[98:113]
	v_mfma_f32_32x32x16_bf16 v[114:129], v[178:181], v[142:145], v[114:129]
	v_mfma_f32_32x32x16_bf16 v[98:113], v[166:169], v[142:145], v[98:113]
	ds_read_b64_tr_b16 v[4:5], v2 offset:0x400
	ds_read_b64_tr_b16 v[6:7], v2 offset:0xc00
	ds_read_b64_tr_b16 v[8:9], v2 offset:0x1400
	ds_read_b64_tr_b16 v[10:11], v2 offset:0x1c00
	ds_read_b64_tr_b16 v[12:13], v2 offset:0x2400
	ds_read_b64_tr_b16 v[14:15], v2 offset:0x2c00
	ds_read_b64_tr_b16 v[162:163], v2 offset:0x3400
	ds_read_b64_tr_b16 v[164:165], v2 offset:0x3c00
	s_waitcnt lgkmcnt(8)
	v_mfma_f32_32x32x16_bf16 v[66:81], v[146:149], v[194:197], v[66:81]
	v_mfma_f32_32x32x16_bf16 v[66:81], v[150:153], v[190:193], v[66:81]
	v_mfma_f32_32x32x16_bf16 v[66:81], v[154:157], v[186:189], v[66:81]
	v_mfma_f32_32x32x16_bf16 v[66:81], v[158:161], v[182:185], v[66:81]
	ds_read_b64_tr_b16 v[166:167], v2 offset:0x600
	ds_read_b64_tr_b16 v[168:169], v2 offset:0xe00
	ds_read_b64_tr_b16 v[170:171], v2 offset:0x1600
	ds_read_b64_tr_b16 v[172:173], v2 offset:0x1e00
	ds_read_b64_tr_b16 v[174:175], v2 offset:0x2600
	ds_read_b64_tr_b16 v[176:177], v2 offset:0x2e00
	ds_read_b64_tr_b16 v[178:179], v2 offset:0x3600
	ds_read_b64_tr_b16 v[180:181], v2 offset:0x3e00
	s_waitcnt lgkmcnt(8)
	v_mfma_f32_32x32x16_bf16 v[50:65], v[146:149], v[4:7], v[50:65]
	v_mfma_f32_32x32x16_bf16 v[50:65], v[150:153], v[8:11], v[50:65]
	v_mfma_f32_32x32x16_bf16 v[50:65], v[154:157], v[12:15], v[50:65]
	v_mfma_f32_32x32x16_bf16 v[50:65], v[158:161], v[162:165], v[50:65]
	s_waitcnt lgkmcnt(0)
	v_mfma_f32_32x32x16_bf16 v[34:49], v[146:149], v[166:169], v[34:49]
	v_mfma_f32_32x32x16_bf16 v[34:49], v[150:153], v[170:173], v[34:49]
	v_mfma_f32_32x32x16_bf16 v[34:49], v[154:157], v[174:177], v[34:49]
	v_mfma_f32_32x32x16_bf16 v[34:49], v[158:161], v[178:181], v[34:49]
	s_and_b64 vcc, exec, s[6:7]
	s_cbranch_vccnz .LBB0_541
	s_mov_b64 s[10:11], -1
	s_and_b64 vcc, exec, s[96:97]
	s_cbranch_vccz .LBB0_539
	s_waitcnt vmcnt(0)
	s_mov_b64 s[10:11], 0

.LBB0_962:
	s_ashr_i32 s27, s26, 31
	s_lshl_b64 s[28:29], s[26:27], 20
	s_add_u32 s28, s10, s28
	s_addc_u32 s29, s11, s29
	s_ashr_i32 s25, s24, 31
	s_lshl_b64 s[30:31], s[24:25], 20
	s_add_u32 s30, s14, s30
	v_cmp_lt_i64_e64 s[8:9], s[8:9], v[158:159]
	s_addc_u32 s31, s15, s31
	s_andn2_b64 vcc, exec, s[20:21]
	s_cbranch_vccnz .LBB0_954
	s_and_b64 s[8:9], s[8:9], exec
	s_cselect_b32 s25, s29, s39
	s_cselect_b32 s27, s28, s38
	s_cselect_b32 s51, s31, s37
	s_cselect_b32 s52, s30, s36
	s_add_u32 s8, s38, 0x80080
	s_addc_u32 s9, s39, 0
	s_add_u32 s53, s36, 0x100
	v_mov_b32_e32 v2, 0
	s_addc_u32 s54, s37, 0
	s_mov_b32 s36, 0
	ds_read_b128 v[130:133], v172
	ds_read_b128 v[134:137], v172 offset:1024
	ds_read_b128 v[138:141], v172 offset:2048
	ds_read_b128 v[142:145], v172 offset:3072
	s_add_i32 s55, s36, 2
	s_add_u32 s37, s8, 0xfff80080
	s_addc_u32 s38, s9, -1
	s_cmp_eq_u32 s46, s36
	s_cselect_b32 s36, s52, s53
	s_cselect_b32 s39, s25, s38
	s_cselect_b32 s38, s27, s37
	s_cselect_b32 s37, s51, s54
	v_lshl_add_u64 v[200:201], s[8:9], 0, v[154:155]
	s_add_i32 m0, s23, 0xc000
	ds_read_b128 v[162:165], v173
	ds_read_b128 v[166:169], v173 offset:1024
	ds_read_b128 v[176:179], v173 offset:2048
	ds_read_b128 v[180:183], v173 offset:3072
	ds_read_b128 v[184:187], v173 offset:4096
	ds_read_b128 v[188:191], v173 offset:5120
	ds_read_b128 v[192:195], v173 offset:6144
	ds_read_b128 v[196:199], v173 offset:7168
	global_load_lds_dwordx4 v[200:201], off
	v_lshl_add_u64 v[200:201], s[8:9], 0, v[156:157]
	s_add_i32 m0, s23, 0xe000
	s_nop 0
	global_load_lds_dwordx4 v[200:201], off
	s_waitcnt lgkmcnt(8)
	s_barrier
	s_waitcnt lgkmcnt(0)
	s_setprio 1
	s_waitcnt lgkmcnt(0)
	v_mfma_f32_16x16x32_bf16 v[126:129], v[130:133], v[162:165], 0
	v_mfma_f32_16x16x32_bf16 v[122:125], v[138:141], v[162:165], 0
	v_mfma_f32_16x16x32_bf16 v[110:113], v[130:133], v[176:179], 0
	v_mfma_f32_16x16x32_bf16 v[106:109], v[138:141], v[176:179], 0
	v_mfma_f32_16x16x32_bf16 v[94:97], v[130:133], v[184:187], 0
	v_mfma_f32_16x16x32_bf16 v[90:93], v[138:141], v[184:187], 0
	v_mfma_f32_16x16x32_bf16 v[78:81], v[130:133], v[192:195], 0
	v_mfma_f32_16x16x32_bf16 v[74:77], v[138:141], v[192:195], 0
	v_mfma_f32_16x16x32_bf16 v[126:129], v[134:137], v[166:169], v[126:129]
	v_mfma_f32_16x16x32_bf16 v[122:125], v[142:145], v[166:169], v[122:125]
	v_mfma_f32_16x16x32_bf16 v[110:113], v[134:137], v[180:183], v[110:113]
	v_mfma_f32_16x16x32_bf16 v[106:109], v[142:145], v[180:183], v[106:109]
	v_mfma_f32_16x16x32_bf16 v[94:97], v[134:137], v[188:191], v[94:97]
	v_mfma_f32_16x16x32_bf16 v[90:93], v[142:145], v[188:191], v[90:93]
	v_mfma_f32_16x16x32_bf16 v[78:81], v[134:137], v[196:199], v[78:81]
	v_mfma_f32_16x16x32_bf16 v[74:77], v[142:145], v[196:199], v[74:77]
	s_setprio 0
	s_barrier
	s_add_i32 s56, s48, s5
	v_lshl_add_u64 v[218:219], s[36:37], 0, v[148:149]
	s_mov_b32 m0, s56
	ds_read_b128 v[200:203], v174
	ds_read_b128 v[204:207], v174 offset:1024
	ds_read_b128 v[208:211], v174 offset:2048
	ds_read_b128 v[214:217], v174 offset:3072
	global_load_lds_dwordx4 v[218:219], off
	v_lshl_add_u64 v[220:221], s[36:37], 0, v[152:153]
	s_add_i32 m0, s56, 0x2000
	s_nop 0
	global_load_lds_dwordx4 v[220:221], off
	s_barrier
	s_waitcnt lgkmcnt(0)
	s_setprio 1
	s_waitcnt lgkmcnt(0)
	v_mfma_f32_16x16x32_bf16 v[118:121], v[200:203], v[162:165], 0
	v_mfma_f32_16x16x32_bf16 v[114:117], v[208:211], v[162:165], 0
	v_mfma_f32_16x16x32_bf16 v[102:105], v[200:203], v[176:179], 0
	v_mfma_f32_16x16x32_bf16 v[98:101], v[208:211], v[176:179], 0
	v_mfma_f32_16x16x32_bf16 v[86:89], v[200:203], v[184:187], 0
	v_mfma_f32_16x16x32_bf16 v[82:85], v[208:211], v[184:187], 0
	v_mfma_f32_16x16x32_bf16 v[70:73], v[200:203], v[192:195], 0
	v_mfma_f32_16x16x32_bf16 v[66:69], v[208:211], v[192:195], 0
	v_mfma_f32_16x16x32_bf16 v[118:121], v[204:207], v[166:169], v[118:121]
	v_mfma_f32_16x16x32_bf16 v[114:117], v[214:217], v[166:169], v[114:117]
	v_mfma_f32_16x16x32_bf16 v[102:105], v[204:207], v[180:183], v[102:105]
	v_mfma_f32_16x16x32_bf16 v[98:101], v[214:217], v[180:183], v[98:101]
	v_mfma_f32_16x16x32_bf16 v[86:89], v[204:207], v[188:191], v[86:89]
	v_mfma_f32_16x16x32_bf16 v[82:85], v[214:217], v[188:191], v[82:85]
	v_mfma_f32_16x16x32_bf16 v[70:73], v[204:207], v[196:199], v[70:73]
	v_mfma_f32_16x16x32_bf16 v[66:69], v[214:217], v[196:199], v[66:69]
	s_setprio 0
	s_mov_b32 m0, s23
	v_lshl_add_u64 v[222:223], s[38:39], 0, v[146:147]
	s_barrier
	ds_read_b128 v[162:165], v173 offset:16384
	ds_read_b128 v[166:169], v173 offset:17408
	ds_read_b128 v[176:179], v173 offset:18432
	ds_read_b128 v[180:183], v173 offset:19456
	ds_read_b128 v[184:187], v173 offset:20480
	ds_read_b128 v[188:191], v173 offset:21504
	ds_read_b128 v[192:195], v173 offset:22528
	ds_read_b128 v[196:199], v173 offset:23552
	global_load_lds_dwordx4 v[222:223], off
	v_lshl_add_u64 v[224:225], s[38:39], 0, v[150:151]
	s_mov_b32 m0, s33
	s_nop 0
	global_load_lds_dwordx4 v[224:225], off
	s_barrier
	s_waitcnt lgkmcnt(0)
	s_setprio 1
	s_waitcnt lgkmcnt(0)
	v_mfma_f32_16x16x32_bf16 v[62:65], v[130:133], v[162:165], 0
	v_mfma_f32_16x16x32_bf16 v[58:61], v[138:141], v[162:165], 0
	v_mfma_f32_16x16x32_bf16 v[46:49], v[130:133], v[176:179], 0
	v_mfma_f32_16x16x32_bf16 v[42:45], v[138:141], v[176:179], 0
	v_mfma_f32_16x16x32_bf16 v[30:33], v[130:133], v[184:187], 0
	v_mfma_f32_16x16x32_bf16 v[26:29], v[138:141], v[184:187], 0
	v_mfma_f32_16x16x32_bf16 v[14:17], v[130:133], v[192:195], 0
	v_mfma_f32_16x16x32_bf16 v[10:13], v[138:141], v[192:195], 0
	v_mfma_f32_16x16x32_bf16 v[62:65], v[134:137], v[166:169], v[62:65]
	v_mfma_f32_16x16x32_bf16 v[58:61], v[142:145], v[166:169], v[58:61]
	v_mfma_f32_16x16x32_bf16 v[46:49], v[134:137], v[180:183], v[46:49]
	v_mfma_f32_16x16x32_bf16 v[42:45], v[142:145], v[180:183], v[42:45]
	v_mfma_f32_16x16x32_bf16 v[30:33], v[134:137], v[188:191], v[30:33]
	v_mfma_f32_16x16x32_bf16 v[26:29], v[142:145], v[188:191], v[26:29]
	v_mfma_f32_16x16x32_bf16 v[14:17], v[134:137], v[196:199], v[14:17]
	v_mfma_f32_16x16x32_bf16 v[10:13], v[142:145], v[196:199], v[10:13]
	s_setprio 0
	s_barrier
	s_add_u32 s56, s36, 0x80000
	s_addc_u32 s57, s37, 0
	s_add_i32 s58, s49, s5
	v_lshl_add_u64 v[130:131], s[56:57], 0, v[148:149]
	s_mov_b32 m0, s58
	s_nop 0
	global_load_lds_dwordx4 v[130:131], off
	v_lshl_add_u64 v[130:131], s[56:57], 0, v[152:153]
	s_add_i32 m0, s58, 0x2000
	s_nop 0
	global_load_lds_dwordx4 v[130:131], off
	s_waitcnt vmcnt(6)
	s_barrier
	s_setprio 1
	v_mfma_f32_16x16x32_bf16 v[54:57], v[200:203], v[162:165], 0
	v_mfma_f32_16x16x32_bf16 v[50:53], v[208:211], v[162:165], 0
	v_mfma_f32_16x16x32_bf16 v[38:41], v[200:203], v[176:179], 0
	v_mfma_f32_16x16x32_bf16 v[34:37], v[208:211], v[176:179], 0
	v_mfma_f32_16x16x32_bf16 v[22:25], v[200:203], v[184:187], 0
	v_mfma_f32_16x16x32_bf16 v[18:21], v[208:211], v[184:187], 0
	v_mfma_f32_16x16x32_bf16 v[6:9], v[200:203], v[192:195], 0
	v_mfma_f32_16x16x32_bf16 v[2:5], v[208:211], v[192:195], 0
	v_mfma_f32_16x16x32_bf16 v[54:57], v[204:207], v[166:169], v[54:57]
	v_mfma_f32_16x16x32_bf16 v[50:53], v[214:217], v[166:169], v[50:53]
	v_mfma_f32_16x16x32_bf16 v[38:41], v[204:207], v[180:183], v[38:41]
	v_mfma_f32_16x16x32_bf16 v[34:37], v[214:217], v[180:183], v[34:37]
	v_mfma_f32_16x16x32_bf16 v[22:25], v[204:207], v[188:191], v[22:25]
	v_mfma_f32_16x16x32_bf16 v[18:21], v[214:217], v[188:191], v[18:21]
	v_mfma_f32_16x16x32_bf16 v[6:9], v[204:207], v[196:199], v[6:9]
	v_mfma_f32_16x16x32_bf16 v[2:5], v[214:217], v[196:199], v[2:5]
	s_setprio 0
	s_add_i32 s56, 0, 0x18000
	v_add_u32_e32 v142, s56, v171
	s_barrier
	ds_read_b128 v[130:133], v142
	ds_read_b128 v[134:137], v142 offset:1024
	ds_read_b128 v[138:141], v142 offset:2048
	ds_read_b128 v[142:145], v142 offset:3072
	s_add_u32 s38, s38, 0x80000
	s_addc_u32 s39, s39, 0
	s_mov_b32 m0, s35
	v_lshl_add_u64 v[200:201], s[38:39], 0, v[146:147]
	ds_read_b128 v[162:165], v173 offset:32768
	ds_read_b128 v[166:169], v173 offset:33792
	ds_read_b128 v[176:179], v173 offset:34816
	ds_read_b128 v[180:183], v173 offset:35840
	ds_read_b128 v[184:187], v173 offset:36864
	ds_read_b128 v[188:191], v173 offset:37888
	ds_read_b128 v[192:195], v173 offset:38912
	ds_read_b128 v[196:199], v173 offset:39936
	global_load_lds_dwordx4 v[200:201], off
	v_lshl_add_u64 v[200:201], s[38:39], 0, v[150:151]
	s_mov_b32 m0, s40
	s_nop 0
	global_load_lds_dwordx4 v[200:201], off
	s_waitcnt lgkmcnt(8)
	s_barrier
	s_waitcnt lgkmcnt(0)
	s_setprio 1
	s_waitcnt lgkmcnt(0)
	v_mfma_f32_16x16x32_bf16 v[126:129], v[130:133], v[162:165], v[126:129]
	v_mfma_f32_16x16x32_bf16 v[122:125], v[138:141], v[162:165], v[122:125]
	v_mfma_f32_16x16x32_bf16 v[110:113], v[130:133], v[176:179], v[110:113]
	v_mfma_f32_16x16x32_bf16 v[106:109], v[138:141], v[176:179], v[106:109]
	v_mfma_f32_16x16x32_bf16 v[94:97], v[130:133], v[184:187], v[94:97]
	v_mfma_f32_16x16x32_bf16 v[90:93], v[138:141], v[184:187], v[90:93]
	v_mfma_f32_16x16x32_bf16 v[78:81], v[130:133], v[192:195], v[78:81]
	v_mfma_f32_16x16x32_bf16 v[74:77], v[138:141], v[192:195], v[74:77]
	v_mfma_f32_16x16x32_bf16 v[126:129], v[134:137], v[166:169], v[126:129]
	v_mfma_f32_16x16x32_bf16 v[122:125], v[142:145], v[166:169], v[122:125]
	v_mfma_f32_16x16x32_bf16 v[110:113], v[134:137], v[180:183], v[110:113]
	v_mfma_f32_16x16x32_bf16 v[106:109], v[142:145], v[180:183], v[106:109]
	v_mfma_f32_16x16x32_bf16 v[94:97], v[134:137], v[188:191], v[94:97]
	v_mfma_f32_16x16x32_bf16 v[90:93], v[142:145], v[188:191], v[90:93]
	v_mfma_f32_16x16x32_bf16 v[78:81], v[134:137], v[196:199], v[78:81]
	v_mfma_f32_16x16x32_bf16 v[74:77], v[142:145], v[196:199], v[74:77]
	s_setprio 0
	s_barrier
	s_add_i32 s38, 0, 0x1c000
	s_add_i32 s39, s56, s5
	v_add_u32_e32 v175, s38, v171
	v_lshl_add_u64 v[218:219], v[218:219], 0, s[18:19]
	s_mov_b32 m0, s39
	ds_read_b128 v[200:203], v175
	ds_read_b128 v[204:207], v175 offset:1024
	ds_read_b128 v[208:211], v175 offset:2048
	ds_read_b128 v[214:217], v175 offset:3072
	global_load_lds_dwordx4 v[218:219], off
	v_lshl_add_u64 v[218:219], v[220:221], 0, s[18:19]
	s_add_i32 m0, s39, 0x2000
	s_nop 0
	global_load_lds_dwordx4 v[218:219], off
	s_barrier
	s_waitcnt lgkmcnt(0)
	s_setprio 1
	s_waitcnt lgkmcnt(0)
	v_mfma_f32_16x16x32_bf16 v[118:121], v[200:203], v[162:165], v[118:121]
	v_mfma_f32_16x16x32_bf16 v[114:117], v[208:211], v[162:165], v[114:117]
	v_mfma_f32_16x16x32_bf16 v[102:105], v[200:203], v[176:179], v[102:105]
	v_mfma_f32_16x16x32_bf16 v[98:101], v[208:211], v[176:179], v[98:101]
	v_mfma_f32_16x16x32_bf16 v[86:89], v[200:203], v[184:187], v[86:89]
	v_mfma_f32_16x16x32_bf16 v[82:85], v[208:211], v[184:187], v[82:85]
	v_mfma_f32_16x16x32_bf16 v[70:73], v[200:203], v[192:195], v[70:73]
	v_mfma_f32_16x16x32_bf16 v[66:69], v[208:211], v[192:195], v[66:69]
	v_mfma_f32_16x16x32_bf16 v[118:121], v[204:207], v[166:169], v[118:121]
	v_mfma_f32_16x16x32_bf16 v[114:117], v[214:217], v[166:169], v[114:117]
	v_mfma_f32_16x16x32_bf16 v[102:105], v[204:207], v[180:183], v[102:105]
	v_mfma_f32_16x16x32_bf16 v[98:101], v[214:217], v[180:183], v[98:101]
	v_mfma_f32_16x16x32_bf16 v[86:89], v[204:207], v[188:191], v[86:89]
	v_mfma_f32_16x16x32_bf16 v[82:85], v[214:217], v[188:191], v[82:85]
	v_mfma_f32_16x16x32_bf16 v[70:73], v[204:207], v[196:199], v[70:73]
	v_mfma_f32_16x16x32_bf16 v[66:69], v[214:217], v[196:199], v[66:69]
	s_setprio 0
	s_mov_b32 m0, s44
	v_lshl_add_u64 v[218:219], v[222:223], 0, s[18:19]
	s_barrier
	ds_read_b128 v[162:165], v173 offset:49152
	ds_read_b128 v[166:169], v173 offset:50176
	ds_read_b128 v[176:179], v173 offset:51200
	ds_read_b128 v[180:183], v173 offset:52224
	ds_read_b128 v[184:187], v173 offset:53248
	ds_read_b128 v[188:191], v173 offset:54272
	ds_read_b128 v[192:195], v173 offset:55296
	ds_read_b128 v[196:199], v173 offset:56320
	global_load_lds_dwordx4 v[218:219], off
	v_lshl_add_u64 v[218:219], v[224:225], 0, s[18:19]
	s_mov_b32 m0, s45
	s_nop 0
	global_load_lds_dwordx4 v[218:219], off
	s_barrier
	s_waitcnt lgkmcnt(0)
	s_setprio 1
	s_waitcnt lgkmcnt(0)
	v_mfma_f32_16x16x32_bf16 v[62:65], v[130:133], v[162:165], v[62:65]
	v_mfma_f32_16x16x32_bf16 v[58:61], v[138:141], v[162:165], v[58:61]
	v_mfma_f32_16x16x32_bf16 v[46:49], v[130:133], v[176:179], v[46:49]
	v_mfma_f32_16x16x32_bf16 v[42:45], v[138:141], v[176:179], v[42:45]
	v_mfma_f32_16x16x32_bf16 v[30:33], v[130:133], v[184:187], v[30:33]
	v_mfma_f32_16x16x32_bf16 v[26:29], v[138:141], v[184:187], v[26:29]
	v_mfma_f32_16x16x32_bf16 v[14:17], v[130:133], v[192:195], v[14:17]
	v_mfma_f32_16x16x32_bf16 v[10:13], v[138:141], v[192:195], v[10:13]
	v_mfma_f32_16x16x32_bf16 v[62:65], v[134:137], v[166:169], v[62:65]
	v_mfma_f32_16x16x32_bf16 v[58:61], v[142:145], v[166:169], v[58:61]
	v_mfma_f32_16x16x32_bf16 v[46:49], v[134:137], v[180:183], v[46:49]
	v_mfma_f32_16x16x32_bf16 v[42:45], v[142:145], v[180:183], v[42:45]
	v_mfma_f32_16x16x32_bf16 v[30:33], v[134:137], v[188:191], v[30:33]
	v_mfma_f32_16x16x32_bf16 v[26:29], v[142:145], v[188:191], v[26:29]
	v_mfma_f32_16x16x32_bf16 v[14:17], v[134:137], v[196:199], v[14:17]
	v_mfma_f32_16x16x32_bf16 v[10:13], v[142:145], v[196:199], v[10:13]
	s_setprio 0
	s_barrier
	s_add_u32 s36, s36, 0x80080
	s_addc_u32 s37, s37, 0
	s_add_i32 s38, s38, s5
	v_lshl_add_u64 v[130:131], s[36:37], 0, v[148:149]
	s_mov_b32 m0, s38
	s_nop 0
	global_load_lds_dwordx4 v[130:131], off
	v_lshl_add_u64 v[130:131], s[36:37], 0, v[152:153]
	s_add_i32 m0, s38, 0x2000
	s_nop 0
	global_load_lds_dwordx4 v[130:131], off
	s_waitcnt vmcnt(6)
	s_barrier
	s_setprio 1
	v_mfma_f32_16x16x32_bf16 v[54:57], v[200:203], v[162:165], v[54:57]
	v_mfma_f32_16x16x32_bf16 v[50:53], v[208:211], v[162:165], v[50:53]
	v_mfma_f32_16x16x32_bf16 v[38:41], v[200:203], v[176:179], v[38:41]
	v_mfma_f32_16x16x32_bf16 v[34:37], v[208:211], v[176:179], v[34:37]
	v_mfma_f32_16x16x32_bf16 v[22:25], v[200:203], v[184:187], v[22:25]
	v_mfma_f32_16x16x32_bf16 v[18:21], v[208:211], v[184:187], v[18:21]
	v_mfma_f32_16x16x32_bf16 v[6:9], v[200:203], v[192:195], v[6:9]
	v_mfma_f32_16x16x32_bf16 v[2:5], v[208:211], v[192:195], v[2:5]
	v_mfma_f32_16x16x32_bf16 v[54:57], v[204:207], v[166:169], v[54:57]
	v_mfma_f32_16x16x32_bf16 v[50:53], v[214:217], v[166:169], v[50:53]
	v_mfma_f32_16x16x32_bf16 v[38:41], v[204:207], v[180:183], v[38:41]
	v_mfma_f32_16x16x32_bf16 v[34:37], v[214:217], v[180:183], v[34:37]
	v_mfma_f32_16x16x32_bf16 v[22:25], v[204:207], v[188:191], v[22:25]
	v_mfma_f32_16x16x32_bf16 v[18:21], v[214:217], v[188:191], v[18:21]
	v_mfma_f32_16x16x32_bf16 v[6:9], v[204:207], v[196:199], v[6:9]
	v_mfma_f32_16x16x32_bf16 v[2:5], v[214:217], v[196:199], v[2:5]
	s_setprio 0
	s_add_u32 s8, s8, 0x100
	s_addc_u32 s9, s9, 0
	s_add_u32 s53, s53, 0x100
	s_addc_u32 s54, s54, 0
	s_cmp_ge_i32 s55, s1
	s_mov_b32 s36, s55
	s_barrier
	s_cbranch_scc0 .LBB0_964
	s_branch .Lmy_pl1_exit

.Lmy_pl1_exit:
	s_branch .LBB0_955

.LBB0_1549:
	s_ashr_i32 s25, s15, 31
	s_mov_b32 s24, s15
	s_lshl_b64 s[24:25], s[24:25], 19
	s_add_u32 s24, s16, s24
	s_addc_u32 s25, s17, s25
	s_and_b64 vcc, exec, s[10:11]
	s_cbranch_vccnz .LBB0_1545
	s_and_b64 s[30:31], s[26:27], exec
	s_cselect_b32 s67, s25, s29
	s_cselect_b32 s68, s24, s28
	s_lshl_b32 s30, s64, 11
	s_add_i32 s30, s30, 0
	s_add_i32 s30, s30, 0x20400
	s_add_u32 s69, s28, 0x100
	v_mov_b32_e32 v50, 0
	v_add3_u32 v179, s30, v198, v199
	v_add3_u32 v180, s30, v200, v201
	s_addc_u32 s70, s29, 0
	s_mov_b32 s71, 0
	s_mov_b64 s[28:29], 0
	ds_read_b128 v[2:5], v206
	ds_read_b128 v[10:13], v206 offset:2048
	ds_read_b128 v[6:9], v207
	ds_read_b128 v[14:17], v207 offset:2048
	s_cmp_eq_u32 s51, s71
	s_cselect_b64 s[34:35], -1, 0
	s_add_u32 s30, s53, s28
	s_addc_u32 s31, s54, s29
	s_mov_b32 m0, s55
	ds_read_b128 v[26:29], v208
	ds_read_b128 v[18:21], v208 offset:2048
	ds_read_b128 v[30:33], v209
	ds_read_b128 v[22:25], v209 offset:2048
	ds_read_b128 v[42:45], v208 offset:4096
	ds_read_b128 v[34:37], v208 offset:6144
	ds_read_b128 v[46:49], v209 offset:4096
	ds_read_b128 v[38:41], v209 offset:6144
	global_load_lds_dwordx4 v192, s[30:31]
	s_mov_b32 m0, s56
	s_nop 0
	global_load_lds_dwordx4 v194, s[30:31]
	s_waitcnt lgkmcnt(8)
	s_barrier
	s_waitcnt lgkmcnt(0)
	s_setprio 1
	s_setprio 0
	s_barrier
	s_and_b64 s[30:31], s[26:27], s[34:35]
	s_andn2_b64 vcc, exec, s[30:31]
	s_cbranch_vccnz .Lmy_pl2_1553
	ds_read2st64_b32 v[190:191], v179 offset1:2
	ds_read2st64_b32 v[192:193], v180 offset1:2
	s_waitcnt lgkmcnt(0)
	v_add_u32_e32 v184, v190, v1
	v_add_u32_e32 v190, v192, v181
	v_add_u32_e32 v192, v191, v1
	v_add_u32_e32 v194, v193, v181
.Lmy_pl2_1553:
	s_add_i32 s71, s71, 2
	s_add_u32 s30, s28, 0x100
	s_addc_u32 s31, s29, 0
	s_and_b64 s[36:37], s[34:35], exec
	s_cselect_b32 s36, 0, s30
	s_cselect_b32 s37, 0, s31
	s_add_u32 s36, s22, s36
	s_addc_u32 s37, s23, s37
	s_add_u32 s72, s69, s28
	s_addc_u32 s73, s70, s29
	s_and_b64 s[28:29], s[34:35], exec
	s_cselect_b32 s29, s67, s73
	s_cselect_b32 s28, s68, s72
	s_mov_b32 m0, s42
	v_add_u32_e32 v191, s57, v204
	v_lshl_add_u64 v[230:231], s[28:29], 0, v[188:189]
	v_add_u32_e32 v197, s57, v205
	ds_read_b128 v[214:217], v191
	ds_read_b128 v[222:225], v191 offset:2048
	ds_read_b128 v[218:221], v197
	ds_read_b128 v[226:229], v197 offset:2048
	global_load_lds_dwordx4 v[230:231], off
	v_lshl_add_u64 v[232:233], s[28:29], 0, v[186:187]
	s_mov_b32 m0, s43
	s_waitcnt lgkmcnt(0)
	v_mfma_scale_f32_16x16x128_f8f6f4 v[174:177], v[2:9], v[26:33], 0, v211, v210 op_sel_hi:[0,0,0]
	global_load_lds_dwordx4 v[232:233], off
	s_barrier
	s_waitcnt lgkmcnt(0)
	v_mov_b32_e32 v193, v185
	v_mov_b32_e32 v195, v185
	v_mfma_scale_f32_16x16x128_f8f6f4 v[170:173], v[10:17], v[26:33], 0, v211, v210 op_sel_hi:[0,0,0]
	v_mfma_scale_f32_16x16x128_f8f6f4 v[166:169], v[2:9], v[18:25], 0, v211, v210 op_sel_hi:[0,0,0]
	v_mfma_scale_f32_16x16x128_f8f6f4 v[162:165], v[10:17], v[18:25], 0, v211, v210 op_sel_hi:[0,0,0]
	v_mfma_scale_f32_16x16x128_f8f6f4 v[142:145], v[2:9], v[42:49], 0, v211, v210 op_sel_hi:[0,0,0]
	v_mfma_scale_f32_16x16x128_f8f6f4 v[130:133], v[10:17], v[42:49], 0, v211, v210 op_sel_hi:[0,0,0]
	v_mfma_scale_f32_16x16x128_f8f6f4 v[118:121], v[2:9], v[34:41], 0, v211, v210 op_sel_hi:[0,0,0]
	v_mfma_scale_f32_16x16x128_f8f6f4 v[114:117], v[10:17], v[34:41], 0, v211, v210 op_sel_hi:[0,0,0]
	s_setprio 1
	v_mfma_scale_f32_16x16x128_f8f6f4 v[158:161], v[214:221], v[26:33], 0, v211, v210 op_sel_hi:[0,0,0]
	v_mfma_scale_f32_16x16x128_f8f6f4 v[154:157], v[222:229], v[26:33], 0, v211, v210 op_sel_hi:[0,0,0]
	v_mfma_scale_f32_16x16x128_f8f6f4 v[150:153], v[214:221], v[18:25], 0, v211, v210 op_sel_hi:[0,0,0]
	v_mfma_scale_f32_16x16x128_f8f6f4 v[146:149], v[222:229], v[18:25], 0, v211, v210 op_sel_hi:[0,0,0]
	v_mfma_scale_f32_16x16x128_f8f6f4 v[138:141], v[214:221], v[42:49], 0, v211, v210 op_sel_hi:[0,0,0]
	v_mfma_scale_f32_16x16x128_f8f6f4 v[134:137], v[222:229], v[42:49], 0, v211, v210 op_sel_hi:[0,0,0]
	v_mfma_scale_f32_16x16x128_f8f6f4 v[126:129], v[214:221], v[34:41], 0, v211, v210 op_sel_hi:[0,0,0]
	v_mfma_scale_f32_16x16x128_f8f6f4 v[122:125], v[222:229], v[34:41], 0, v211, v210 op_sel_hi:[0,0,0]
	s_setprio 0
	s_mov_b32 m0, s41
	s_barrier
	ds_read_b128 v[18:21], v208 offset:16384
	ds_read_b128 v[26:29], v208 offset:18432
	ds_read_b128 v[22:25], v209 offset:16384
	ds_read_b128 v[30:33], v209 offset:18432
	ds_read_b128 v[34:37], v208 offset:20480
	ds_read_b128 v[42:45], v208 offset:22528
	ds_read_b128 v[38:41], v209 offset:20480
	ds_read_b128 v[46:49], v209 offset:22528
	global_load_lds_dwordx4 v184, s[36:37]
	s_mov_b32 m0, s44
	v_mov_b32_e32 v191, v185
	global_load_lds_dwordx4 v190, s[36:37]
	s_barrier
	s_waitcnt lgkmcnt(0)
	v_lshl_add_u64 v[234:235], s[36:37], 0, v[184:185]
	v_lshl_add_u64 v[236:237], s[36:37], 0, v[190:191]
	s_setprio 1
	s_waitcnt lgkmcnt(0)
	v_mfma_scale_f32_16x16x128_f8f6f4 v[110:113], v[2:9], v[18:25], 0, v211, v210 op_sel_hi:[0,0,0]
	v_mfma_scale_f32_16x16x128_f8f6f4 v[102:105], v[10:17], v[18:25], 0, v211, v210 op_sel_hi:[0,0,0]
	v_mfma_scale_f32_16x16x128_f8f6f4 v[94:97], v[2:9], v[26:33], 0, v211, v210 op_sel_hi:[0,0,0]
	v_mfma_scale_f32_16x16x128_f8f6f4 v[86:89], v[10:17], v[26:33], 0, v211, v210 op_sel_hi:[0,0,0]
	v_mfma_scale_f32_16x16x128_f8f6f4 v[78:81], v[2:9], v[34:41], 0, v211, v210 op_sel_hi:[0,0,0]
	v_mfma_scale_f32_16x16x128_f8f6f4 v[70:73], v[10:17], v[34:41], 0, v211, v210 op_sel_hi:[0,0,0]
	v_mfma_scale_f32_16x16x128_f8f6f4 v[62:65], v[2:9], v[42:49], 0, v211, v210 op_sel_hi:[0,0,0]
	v_mfma_scale_f32_16x16x128_f8f6f4 v[54:57], v[10:17], v[42:49], 0, v211, v210 op_sel_hi:[0,0,0]
	s_setprio 0
	s_barrier
	s_add_u32 s34, s28, 0x40000
	s_addc_u32 s35, s29, 0
	s_mov_b32 m0, s59
	v_lshl_add_u64 v[2:3], s[34:35], 0, v[188:189]
	global_load_lds_dwordx4 v[2:3], off
	v_lshl_add_u64 v[2:3], s[34:35], 0, v[186:187]
	s_mov_b32 m0, s60
	s_nop 0
	global_load_lds_dwordx4 v[2:3], off
	s_waitcnt vmcnt(6)
	s_barrier
	s_setprio 1
	v_mfma_scale_f32_16x16x128_f8f6f4 v[106:109], v[214:221], v[18:25], 0, v211, v210 op_sel_hi:[0,0,0]
	v_mfma_scale_f32_16x16x128_f8f6f4 v[98:101], v[222:229], v[18:25], 0, v211, v210 op_sel_hi:[0,0,0]
	v_mfma_scale_f32_16x16x128_f8f6f4 v[90:93], v[214:221], v[26:33], 0, v211, v210 op_sel_hi:[0,0,0]
	v_mfma_scale_f32_16x16x128_f8f6f4 v[82:85], v[222:229], v[26:33], 0, v211, v210 op_sel_hi:[0,0,0]
	v_mfma_scale_f32_16x16x128_f8f6f4 v[74:77], v[214:221], v[34:41], 0, v211, v210 op_sel_hi:[0,0,0]
	v_mfma_scale_f32_16x16x128_f8f6f4 v[66:69], v[222:229], v[34:41], 0, v211, v210 op_sel_hi:[0,0,0]
	v_mfma_scale_f32_16x16x128_f8f6f4 v[58:61], v[214:221], v[42:49], 0, v211, v210 op_sel_hi:[0,0,0]
	v_mfma_scale_f32_16x16x128_f8f6f4 v[50:53], v[222:229], v[42:49], 0, v211, v210 op_sel_hi:[0,0,0]
	s_setprio 0
	v_add_u32_e32 v6, s61, v204
	v_add_u32_e32 v14, s61, v205
	s_barrier
	ds_read_b128 v[2:5], v6
	ds_read_b128 v[10:13], v6 offset:2048
	ds_read_b128 v[6:9], v14
	ds_read_b128 v[14:17], v14 offset:2048
	s_mov_b32 m0, s45
	v_lshl_add_u64 v[214:215], s[36:37], 0, v[192:193]
	ds_read_b128 v[18:21], v208 offset:32768
	ds_read_b128 v[26:29], v208 offset:34816
	ds_read_b128 v[22:25], v209 offset:32768
	ds_read_b128 v[30:33], v209 offset:34816
	ds_read_b128 v[34:37], v208 offset:36864
	ds_read_b128 v[42:45], v208 offset:38912
	ds_read_b128 v[38:41], v209 offset:36864
	ds_read_b128 v[46:49], v209 offset:38912
	global_load_lds_dwordx4 v[214:215], off
	v_lshl_add_u64 v[214:215], s[36:37], 0, v[194:195]
	s_mov_b32 m0, s46
	s_nop 0
	global_load_lds_dwordx4 v[214:215], off
	s_waitcnt lgkmcnt(8)
	s_barrier
	s_waitcnt lgkmcnt(0)
	s_setprio 1
	s_waitcnt lgkmcnt(0)
	v_mfma_scale_f32_16x16x128_f8f6f4 v[174:177], v[2:9], v[18:25], v[174:177], v211, v210 op_sel_hi:[0,0,0]
	v_mfma_scale_f32_16x16x128_f8f6f4 v[170:173], v[10:17], v[18:25], v[170:173], v211, v210 op_sel_hi:[0,0,0]
	v_mfma_scale_f32_16x16x128_f8f6f4 v[166:169], v[2:9], v[26:33], v[166:169], v211, v210 op_sel_hi:[0,0,0]
	v_mfma_scale_f32_16x16x128_f8f6f4 v[162:165], v[10:17], v[26:33], v[162:165], v211, v210 op_sel_hi:[0,0,0]
	v_mfma_scale_f32_16x16x128_f8f6f4 v[142:145], v[2:9], v[34:41], v[142:145], v211, v210 op_sel_hi:[0,0,0]
	v_mfma_scale_f32_16x16x128_f8f6f4 v[130:133], v[10:17], v[34:41], v[130:133], v211, v210 op_sel_hi:[0,0,0]
	v_mfma_scale_f32_16x16x128_f8f6f4 v[118:121], v[2:9], v[42:49], v[118:121], v211, v210 op_sel_hi:[0,0,0]
	v_mfma_scale_f32_16x16x128_f8f6f4 v[114:117], v[10:17], v[42:49], v[114:117], v211, v210 op_sel_hi:[0,0,0]
	s_setprio 0
	s_barrier
	s_mov_b32 m0, s63
	v_add_u32_e32 v191, s62, v204
	v_lshl_add_u64 v[230:231], v[230:231], 0, s[12:13]
	v_add_u32_e32 v193, s62, v205
	ds_read_b128 v[214:217], v191
	ds_read_b128 v[222:225], v191 offset:2048
	ds_read_b128 v[218:221], v193
	ds_read_b128 v[226:229], v193 offset:2048
	global_load_lds_dwordx4 v[230:231], off
	v_lshl_add_u64 v[230:231], v[232:233], 0, s[12:13]
	s_add_i32 m0, s63, 0x2000
	s_nop 0
	global_load_lds_dwordx4 v[230:231], off
	s_barrier
	s_waitcnt lgkmcnt(0)
	s_setprio 1
	s_waitcnt lgkmcnt(0)
	v_mfma_scale_f32_16x16x128_f8f6f4 v[158:161], v[214:221], v[18:25], v[158:161], v211, v210 op_sel_hi:[0,0,0]
	v_mfma_scale_f32_16x16x128_f8f6f4 v[154:157], v[222:229], v[18:25], v[154:157], v211, v210 op_sel_hi:[0,0,0]
	v_mfma_scale_f32_16x16x128_f8f6f4 v[150:153], v[214:221], v[26:33], v[150:153], v211, v210 op_sel_hi:[0,0,0]
	v_mfma_scale_f32_16x16x128_f8f6f4 v[146:149], v[222:229], v[26:33], v[146:149], v211, v210 op_sel_hi:[0,0,0]
	v_mfma_scale_f32_16x16x128_f8f6f4 v[138:141], v[214:221], v[34:41], v[138:141], v211, v210 op_sel_hi:[0,0,0]
	v_mfma_scale_f32_16x16x128_f8f6f4 v[134:137], v[222:229], v[34:41], v[134:137], v211, v210 op_sel_hi:[0,0,0]
	v_mfma_scale_f32_16x16x128_f8f6f4 v[126:129], v[214:221], v[42:49], v[126:129], v211, v210 op_sel_hi:[0,0,0]
	v_mfma_scale_f32_16x16x128_f8f6f4 v[122:125], v[222:229], v[42:49], v[122:125], v211, v210 op_sel_hi:[0,0,0]
	s_setprio 0
	s_mov_b32 m0, s49
	v_lshl_add_u64 v[230:231], v[234:235], 0, s[12:13]
	s_barrier
	ds_read_b128 v[18:21], v208 offset:49152
	ds_read_b128 v[26:29], v208 offset:51200
	ds_read_b128 v[22:25], v209 offset:49152
	ds_read_b128 v[30:33], v209 offset:51200
	ds_read_b128 v[34:37], v208 offset:53248
	ds_read_b128 v[42:45], v208 offset:55296
	ds_read_b128 v[38:41], v209 offset:53248
	ds_read_b128 v[46:49], v209 offset:55296
	global_load_lds_dwordx4 v[230:231], off
	v_lshl_add_u64 v[230:231], v[236:237], 0, s[12:13]
	s_mov_b32 m0, s50
	s_nop 0
	global_load_lds_dwordx4 v[230:231], off
	s_barrier
	s_waitcnt lgkmcnt(0)
	s_setprio 1
	s_waitcnt lgkmcnt(0)
	v_mfma_scale_f32_16x16x128_f8f6f4 v[110:113], v[2:9], v[18:25], v[110:113], v211, v210 op_sel_hi:[0,0,0]
	v_mfma_scale_f32_16x16x128_f8f6f4 v[102:105], v[10:17], v[18:25], v[102:105], v211, v210 op_sel_hi:[0,0,0]
	v_mfma_scale_f32_16x16x128_f8f6f4 v[94:97], v[2:9], v[26:33], v[94:97], v211, v210 op_sel_hi:[0,0,0]
	v_mfma_scale_f32_16x16x128_f8f6f4 v[86:89], v[10:17], v[26:33], v[86:89], v211, v210 op_sel_hi:[0,0,0]
	v_mfma_scale_f32_16x16x128_f8f6f4 v[78:81], v[2:9], v[34:41], v[78:81], v211, v210 op_sel_hi:[0,0,0]
	v_mfma_scale_f32_16x16x128_f8f6f4 v[70:73], v[10:17], v[34:41], v[70:73], v211, v210 op_sel_hi:[0,0,0]
	v_mfma_scale_f32_16x16x128_f8f6f4 v[62:65], v[2:9], v[42:49], v[62:65], v211, v210 op_sel_hi:[0,0,0]
	v_mfma_scale_f32_16x16x128_f8f6f4 v[54:57], v[10:17], v[42:49], v[54:57], v211, v210 op_sel_hi:[0,0,0]
	s_setprio 0
	s_barrier
	s_add_u32 s28, s28, 0x40080
	s_addc_u32 s29, s29, 0
	s_add_i32 s34, s62, s40
	v_lshl_add_u64 v[2:3], s[28:29], 0, v[188:189]
	s_mov_b32 m0, s34
	s_nop 0
	global_load_lds_dwordx4 v[2:3], off
	v_lshl_add_u64 v[2:3], s[28:29], 0, v[186:187]
	s_add_i32 m0, s34, 0x2000
	s_nop 0
	global_load_lds_dwordx4 v[2:3], off
	s_waitcnt vmcnt(6)
	s_barrier
	s_setprio 1
	v_mfma_scale_f32_16x16x128_f8f6f4 v[106:109], v[214:221], v[18:25], v[106:109], v211, v210 op_sel_hi:[0,0,0]
	v_mfma_scale_f32_16x16x128_f8f6f4 v[98:101], v[222:229], v[18:25], v[98:101], v211, v210 op_sel_hi:[0,0,0]
	v_mfma_scale_f32_16x16x128_f8f6f4 v[90:93], v[214:221], v[26:33], v[90:93], v211, v210 op_sel_hi:[0,0,0]
	v_mfma_scale_f32_16x16x128_f8f6f4 v[82:85], v[222:229], v[26:33], v[82:85], v211, v210 op_sel_hi:[0,0,0]
	v_mfma_scale_f32_16x16x128_f8f6f4 v[74:77], v[214:221], v[34:41], v[74:77], v211, v210 op_sel_hi:[0,0,0]
	v_mfma_scale_f32_16x16x128_f8f6f4 v[66:69], v[222:229], v[34:41], v[66:69], v211, v210 op_sel_hi:[0,0,0]
	v_mfma_scale_f32_16x16x128_f8f6f4 v[58:61], v[214:221], v[42:49], v[58:61], v211, v210 op_sel_hi:[0,0,0]
	v_mfma_scale_f32_16x16x128_f8f6f4 v[50:53], v[222:229], v[42:49], v[50:53], v211, v210 op_sel_hi:[0,0,0]
	s_setprio 0
	s_cmp_ge_i32 s71, s39
	s_barrier
	s_cbranch_scc1 .LBB0_1546
	s_mov_b64 s[28:29], s[30:31]
	s_branch .LBB0_1551

.LBB0_1671:
	s_ashr_i32 s19, s17, 31
	s_mov_b32 s18, s17
	s_lshl_b64 s[18:19], s[18:19], 17
	s_add_u32 s18, s10, s18
	s_addc_u32 s19, s11, s19
	s_and_b64 vcc, exec, s[6:7]
	s_cbranch_vccnz .LBB0_1667
	s_and_b64 s[24:25], s[20:21], exec
	s_cselect_b32 s55, s19, s23
	s_cselect_b32 s56, s18, s22
	s_lshl_b32 s24, s40, 10
	s_add_i32 s24, s24, 0
	s_add_i32 s24, s24, 0x20400
	s_add_u32 s57, s22, 0x100
	v_mov_b32_e32 v50, 0
	v_add3_u32 v179, s24, v196, v197
	v_add3_u32 v180, s24, v198, v199
	s_addc_u32 s58, s23, 0
	s_mov_b32 s59, 0
	s_mov_b64 s[22:23], 0
	ds_read_b128 v[2:5], v204
	ds_read_b128 v[10:13], v204 offset:2048
	ds_read_b128 v[6:9], v205
	ds_read_b128 v[14:17], v205 offset:2048
	s_cmp_eq_u32 s41, s59
	s_cselect_b64 s[26:27], -1, 0
	s_add_u32 s24, s42, s22
	s_addc_u32 s25, s43, s23
	s_mov_b32 m0, s44
	ds_read_b128 v[26:29], v206
	ds_read_b128 v[18:21], v206 offset:2048
	ds_read_b128 v[30:33], v207
	ds_read_b128 v[22:25], v207 offset:2048
	ds_read_b128 v[42:45], v206 offset:4096
	ds_read_b128 v[34:37], v206 offset:6144
	ds_read_b128 v[46:49], v207 offset:4096
	ds_read_b128 v[38:41], v207 offset:6144
	global_load_lds_dwordx4 v192, s[24:25]
	s_mov_b32 m0, s45
	s_nop 0
	global_load_lds_dwordx4 v194, s[24:25]
	s_waitcnt lgkmcnt(8)
	s_barrier
	s_waitcnt lgkmcnt(0)
	s_setprio 1
	s_setprio 0
	s_barrier
	s_and_b64 s[24:25], s[20:21], s[26:27]
	s_andn2_b64 vcc, exec, s[24:25]
	s_cbranch_vccnz .Lmy_pl3_1675
	ds_read2st64_b32 v[190:191], v179 offset1:2
	ds_read2st64_b32 v[192:193], v180 offset1:2
	s_waitcnt lgkmcnt(0)
	v_add_u32_e32 v184, v190, v1
	v_add_u32_e32 v190, v192, v181
	v_add_u32_e32 v192, v191, v1
	v_add_u32_e32 v194, v193, v181
.Lmy_pl3_1675:
	s_add_i32 s59, s59, 2
	s_add_u32 s24, s22, 0x100
	s_addc_u32 s25, s23, 0
	s_and_b64 s[28:29], s[26:27], exec
	s_cselect_b32 s28, 0, s24
	s_cselect_b32 s29, 0, s25
	s_add_u32 s28, s12, s28
	s_addc_u32 s29, s13, s29
	s_add_u32 s60, s57, s22
	s_addc_u32 s61, s58, s23
	s_and_b64 s[22:23], s[26:27], exec
	s_cselect_b32 s23, s55, s61
	s_cselect_b32 s22, s56, s60
	s_mov_b32 m0, s5
	s_waitcnt lgkmcnt(0)
	v_mfma_scale_f32_16x16x128_f8f6f4 v[222:225], v[2:9], v[42:49], 0, v209, v208 op_sel_hi:[0,0,0]
	v_lshl_add_u64 v[238:239], s[22:23], 0, v[188:189]
	v_add_u32_e32 v191, s46, v203
	v_lshl_add_u64 v[240:241], s[22:23], 0, v[186:187]
	v_mov_b32_e32 v193, v185
	v_mov_b32_e32 v195, v185
	s_nop 1
	v_add_u32_e32 v142, s46, v202
	v_mfma_scale_f32_16x16x128_f8f6f4 v[226:229], v[10:17], v[42:49], 0, v209, v208 op_sel_hi:[0,0,0]
	s_nop 6
	ds_read_b128 v[138:141], v142
	ds_read_b128 v[214:217], v142 offset:2048
	ds_read_b128 v[142:145], v191
	ds_read_b128 v[218:221], v191 offset:2048
	global_load_lds_dwordx4 v[238:239], off
	s_mov_b32 m0, s31
	s_nop 0
	global_load_lds_dwordx4 v[240:241], off
	v_mfma_scale_f32_16x16x128_f8f6f4 v[174:177], v[2:9], v[26:33], 0, v209, v208 op_sel_hi:[0,0,0]
	s_barrier
	s_waitcnt lgkmcnt(0)
	v_mfma_scale_f32_16x16x128_f8f6f4 v[170:173], v[10:17], v[26:33], 0, v209, v208 op_sel_hi:[0,0,0]
	v_mfma_scale_f32_16x16x128_f8f6f4 v[166:169], v[2:9], v[18:25], 0, v209, v208 op_sel_hi:[0,0,0]
	v_mfma_scale_f32_16x16x128_f8f6f4 v[162:165], v[10:17], v[18:25], 0, v209, v208 op_sel_hi:[0,0,0]
	v_mfma_scale_f32_16x16x128_f8f6f4 v[134:137], v[2:9], v[34:41], 0, v209, v208 op_sel_hi:[0,0,0]
	v_mfma_scale_f32_16x16x128_f8f6f4 v[122:125], v[10:17], v[34:41], 0, v209, v208 op_sel_hi:[0,0,0]
	s_setprio 1
	s_waitcnt lgkmcnt(0)
	v_mfma_scale_f32_16x16x128_f8f6f4 v[158:161], v[138:145], v[26:33], 0, v209, v208 op_sel_hi:[0,0,0]
	v_mfma_scale_f32_16x16x128_f8f6f4 v[154:157], v[214:221], v[26:33], 0, v209, v208 op_sel_hi:[0,0,0]
	v_mfma_scale_f32_16x16x128_f8f6f4 v[150:153], v[138:145], v[18:25], 0, v209, v208 op_sel_hi:[0,0,0]
	v_mfma_scale_f32_16x16x128_f8f6f4 v[146:149], v[214:221], v[18:25], 0, v209, v208 op_sel_hi:[0,0,0]
	v_mfma_scale_f32_16x16x128_f8f6f4 v[130:133], v[138:145], v[42:49], 0, v209, v208 op_sel_hi:[0,0,0]
	v_mfma_scale_f32_16x16x128_f8f6f4 v[126:129], v[214:221], v[42:49], 0, v209, v208 op_sel_hi:[0,0,0]
	v_mfma_scale_f32_16x16x128_f8f6f4 v[118:121], v[138:145], v[34:41], 0, v209, v208 op_sel_hi:[0,0,0]
	v_mfma_scale_f32_16x16x128_f8f6f4 v[114:117], v[214:221], v[34:41], 0, v209, v208 op_sel_hi:[0,0,0]
	s_setprio 0
	s_mov_b32 m0, s4
	s_barrier
	ds_read_b128 v[18:21], v206 offset:16384
	ds_read_b128 v[26:29], v206 offset:18432
	ds_read_b128 v[22:25], v207 offset:16384
	ds_read_b128 v[30:33], v207 offset:18432
	ds_read_b128 v[34:37], v206 offset:20480
	ds_read_b128 v[42:45], v206 offset:22528
	ds_read_b128 v[38:41], v207 offset:20480
	ds_read_b128 v[46:49], v207 offset:22528
	global_load_lds_dwordx4 v184, s[28:29]
	s_mov_b32 m0, s33
	v_mov_b32_e32 v191, v185
	global_load_lds_dwordx4 v190, s[28:29]
	s_barrier
	s_waitcnt lgkmcnt(0)
	v_lshl_add_u64 v[242:243], s[28:29], 0, v[184:185]
	v_lshl_add_u64 v[244:245], s[28:29], 0, v[190:191]
	s_setprio 1
	s_waitcnt lgkmcnt(0)
	v_mfma_scale_f32_16x16x128_f8f6f4 v[110:113], v[2:9], v[18:25], 0, v209, v208 op_sel_hi:[0,0,0]
	v_mfma_scale_f32_16x16x128_f8f6f4 v[106:109], v[10:17], v[18:25], 0, v209, v208 op_sel_hi:[0,0,0]
	v_mfma_scale_f32_16x16x128_f8f6f4 v[102:105], v[2:9], v[26:33], 0, v209, v208 op_sel_hi:[0,0,0]
	v_mfma_scale_f32_16x16x128_f8f6f4 v[98:101], v[10:17], v[26:33], 0, v209, v208 op_sel_hi:[0,0,0]
	v_mfma_scale_f32_16x16x128_f8f6f4 v[78:81], v[2:9], v[34:41], 0, v209, v208 op_sel_hi:[0,0,0]
	v_mfma_scale_f32_16x16x128_f8f6f4 v[74:77], v[10:17], v[34:41], 0, v209, v208 op_sel_hi:[0,0,0]
	v_mfma_scale_f32_16x16x128_f8f6f4 v[70:73], v[2:9], v[42:49], 0, v209, v208 op_sel_hi:[0,0,0]
	v_mfma_scale_f32_16x16x128_f8f6f4 v[66:69], v[10:17], v[42:49], 0, v209, v208 op_sel_hi:[0,0,0]
	s_setprio 0
	s_barrier
	s_add_u32 s26, s22, 0x10000
	s_addc_u32 s27, s23, 0
	s_mov_b32 m0, s48
	v_lshl_add_u64 v[2:3], s[26:27], 0, v[188:189]
	global_load_lds_dwordx4 v[2:3], off
	v_lshl_add_u64 v[2:3], s[26:27], 0, v[186:187]
	s_mov_b32 m0, s49
	s_nop 0
	global_load_lds_dwordx4 v[2:3], off
	s_waitcnt vmcnt(6)
	s_barrier
	s_setprio 1
	v_mfma_scale_f32_16x16x128_f8f6f4 v[94:97], v[138:145], v[18:25], 0, v209, v208 op_sel_hi:[0,0,0]
	v_mfma_scale_f32_16x16x128_f8f6f4 v[90:93], v[214:221], v[18:25], 0, v209, v208 op_sel_hi:[0,0,0]
	v_mfma_scale_f32_16x16x128_f8f6f4 v[86:89], v[138:145], v[26:33], 0, v209, v208 op_sel_hi:[0,0,0]
	v_mfma_scale_f32_16x16x128_f8f6f4 v[82:85], v[214:221], v[26:33], 0, v209, v208 op_sel_hi:[0,0,0]
	v_mfma_scale_f32_16x16x128_f8f6f4 v[62:65], v[138:145], v[34:41], 0, v209, v208 op_sel_hi:[0,0,0]
	v_mfma_scale_f32_16x16x128_f8f6f4 v[58:61], v[214:221], v[34:41], 0, v209, v208 op_sel_hi:[0,0,0]
	v_mfma_scale_f32_16x16x128_f8f6f4 v[230:233], v[138:145], v[42:49], 0, v209, v208 op_sel_hi:[0,0,0]
	v_mfma_scale_f32_16x16x128_f8f6f4 v[234:237], v[214:221], v[42:49], 0, v209, v208 op_sel_hi:[0,0,0]
	s_setprio 0
	v_add_u32_e32 v6, s50, v202
	v_add_u32_e32 v14, s50, v203
	s_barrier
	ds_read_b128 v[2:5], v6
	ds_read_b128 v[10:13], v6 offset:2048
	ds_read_b128 v[6:9], v14
	ds_read_b128 v[14:17], v14 offset:2048
	s_mov_b32 m0, s34
	v_lshl_add_u64 v[50:51], s[28:29], 0, v[192:193]
	ds_read_b128 v[18:21], v206 offset:32768
	ds_read_b128 v[26:29], v206 offset:34816
	ds_read_b128 v[22:25], v207 offset:32768
	ds_read_b128 v[30:33], v207 offset:34816
	ds_read_b128 v[34:37], v206 offset:36864
	ds_read_b128 v[42:45], v206 offset:38912
	ds_read_b128 v[38:41], v207 offset:36864
	ds_read_b128 v[46:49], v207 offset:38912
	global_load_lds_dwordx4 v[50:51], off
	v_lshl_add_u64 v[50:51], s[28:29], 0, v[194:195]
	s_mov_b32 m0, s35
	s_nop 0
	global_load_lds_dwordx4 v[50:51], off
	s_waitcnt lgkmcnt(8)
	s_barrier
	s_waitcnt lgkmcnt(0)
	s_setprio 1
	s_waitcnt lgkmcnt(0)
	v_mfma_scale_f32_16x16x128_f8f6f4 v[174:177], v[2:9], v[18:25], v[174:177], v209, v208 op_sel_hi:[0,0,0]
	v_mfma_scale_f32_16x16x128_f8f6f4 v[170:173], v[10:17], v[18:25], v[170:173], v209, v208 op_sel_hi:[0,0,0]
	v_mfma_scale_f32_16x16x128_f8f6f4 v[166:169], v[2:9], v[26:33], v[166:169], v209, v208 op_sel_hi:[0,0,0]
	v_mfma_scale_f32_16x16x128_f8f6f4 v[162:165], v[10:17], v[26:33], v[162:165], v209, v208 op_sel_hi:[0,0,0]
	v_mfma_scale_f32_16x16x128_f8f6f4 v[142:145], v[2:9], v[34:41], v[222:225], v209, v208 op_sel_hi:[0,0,0]
	v_mfma_scale_f32_16x16x128_f8f6f4 v[138:141], v[10:17], v[34:41], v[226:229], v209, v208 op_sel_hi:[0,0,0]
	v_mfma_scale_f32_16x16x128_f8f6f4 v[134:137], v[2:9], v[42:49], v[134:137], v209, v208 op_sel_hi:[0,0,0]
	v_mfma_scale_f32_16x16x128_f8f6f4 v[122:125], v[10:17], v[42:49], v[122:125], v209, v208 op_sel_hi:[0,0,0]
	s_setprio 0
	s_barrier
	s_mov_b32 m0, s52
	v_add_u32_e32 v54, s51, v202
	v_lshl_add_u64 v[222:223], v[238:239], 0, s[8:9]
	v_add_u32_e32 v191, s51, v203
	ds_read_b128 v[50:53], v54
	ds_read_b128 v[214:217], v54 offset:2048
	ds_read_b128 v[54:57], v191
	ds_read_b128 v[218:221], v191 offset:2048
	global_load_lds_dwordx4 v[222:223], off
	v_lshl_add_u64 v[222:223], v[240:241], 0, s[8:9]
	s_mov_b32 m0, s53
	s_nop 0
	global_load_lds_dwordx4 v[222:223], off
	s_barrier
	s_waitcnt lgkmcnt(0)
	s_setprio 1
	s_waitcnt lgkmcnt(0)
	v_mfma_scale_f32_16x16x128_f8f6f4 v[158:161], v[50:57], v[18:25], v[158:161], v209, v208 op_sel_hi:[0,0,0]
	v_mfma_scale_f32_16x16x128_f8f6f4 v[154:157], v[214:221], v[18:25], v[154:157], v209, v208 op_sel_hi:[0,0,0]
	v_mfma_scale_f32_16x16x128_f8f6f4 v[150:153], v[50:57], v[26:33], v[150:153], v209, v208 op_sel_hi:[0,0,0]
	v_mfma_scale_f32_16x16x128_f8f6f4 v[146:149], v[214:221], v[26:33], v[146:149], v209, v208 op_sel_hi:[0,0,0]
	v_mfma_scale_f32_16x16x128_f8f6f4 v[130:133], v[50:57], v[34:41], v[130:133], v209, v208 op_sel_hi:[0,0,0]
	v_mfma_scale_f32_16x16x128_f8f6f4 v[126:129], v[214:221], v[34:41], v[126:129], v209, v208 op_sel_hi:[0,0,0]
	v_mfma_scale_f32_16x16x128_f8f6f4 v[118:121], v[50:57], v[42:49], v[118:121], v209, v208 op_sel_hi:[0,0,0]
	v_mfma_scale_f32_16x16x128_f8f6f4 v[114:117], v[214:221], v[42:49], v[114:117], v209, v208 op_sel_hi:[0,0,0]
	s_setprio 0
	s_mov_b32 m0, s38
	v_lshl_add_u64 v[222:223], v[242:243], 0, s[8:9]
	s_barrier
	ds_read_b128 v[18:21], v206 offset:49152
	ds_read_b128 v[26:29], v206 offset:51200
	ds_read_b128 v[22:25], v207 offset:49152
	ds_read_b128 v[30:33], v207 offset:51200
	ds_read_b128 v[34:37], v206 offset:53248
	ds_read_b128 v[42:45], v206 offset:55296
	ds_read_b128 v[38:41], v207 offset:53248
	ds_read_b128 v[46:49], v207 offset:55296
	global_load_lds_dwordx4 v[222:223], off
	v_lshl_add_u64 v[222:223], v[244:245], 0, s[8:9]
	s_mov_b32 m0, s39
	s_nop 0
	global_load_lds_dwordx4 v[222:223], off
	s_barrier
	s_waitcnt lgkmcnt(0)
	s_setprio 1
	s_waitcnt lgkmcnt(0)
	v_mfma_scale_f32_16x16x128_f8f6f4 v[110:113], v[2:9], v[18:25], v[110:113], v209, v208 op_sel_hi:[0,0,0]
	v_mfma_scale_f32_16x16x128_f8f6f4 v[106:109], v[10:17], v[18:25], v[106:109], v209, v208 op_sel_hi:[0,0,0]
	v_mfma_scale_f32_16x16x128_f8f6f4 v[102:105], v[2:9], v[26:33], v[102:105], v209, v208 op_sel_hi:[0,0,0]
	v_mfma_scale_f32_16x16x128_f8f6f4 v[98:101], v[10:17], v[26:33], v[98:101], v209, v208 op_sel_hi:[0,0,0]
	v_mfma_scale_f32_16x16x128_f8f6f4 v[78:81], v[2:9], v[34:41], v[78:81], v209, v208 op_sel_hi:[0,0,0]
	v_mfma_scale_f32_16x16x128_f8f6f4 v[74:77], v[10:17], v[34:41], v[74:77], v209, v208 op_sel_hi:[0,0,0]
	v_mfma_scale_f32_16x16x128_f8f6f4 v[70:73], v[2:9], v[42:49], v[70:73], v209, v208 op_sel_hi:[0,0,0]
	v_mfma_scale_f32_16x16x128_f8f6f4 v[66:69], v[10:17], v[42:49], v[66:69], v209, v208 op_sel_hi:[0,0,0]
	s_setprio 0
	s_barrier
	s_add_u32 s22, s22, 0x10080
	s_addc_u32 s23, s23, 0
	s_mov_b32 m0, s54
	v_lshl_add_u64 v[2:3], s[22:23], 0, v[188:189]
	global_load_lds_dwordx4 v[2:3], off
	v_lshl_add_u64 v[2:3], s[22:23], 0, v[186:187]
	s_add_i32 m0, s54, 0x2000
	s_nop 0
	global_load_lds_dwordx4 v[2:3], off
	s_waitcnt vmcnt(6)
	s_barrier
	s_setprio 1
	v_mfma_scale_f32_16x16x128_f8f6f4 v[94:97], v[50:57], v[18:25], v[94:97], v209, v208 op_sel_hi:[0,0,0]
	v_mfma_scale_f32_16x16x128_f8f6f4 v[90:93], v[214:221], v[18:25], v[90:93], v209, v208 op_sel_hi:[0,0,0]
	v_mfma_scale_f32_16x16x128_f8f6f4 v[86:89], v[50:57], v[26:33], v[86:89], v209, v208 op_sel_hi:[0,0,0]
	v_mfma_scale_f32_16x16x128_f8f6f4 v[82:85], v[214:221], v[26:33], v[82:85], v209, v208 op_sel_hi:[0,0,0]
	v_mfma_scale_f32_16x16x128_f8f6f4 v[62:65], v[50:57], v[34:41], v[62:65], v209, v208 op_sel_hi:[0,0,0]
	v_mfma_scale_f32_16x16x128_f8f6f4 v[58:61], v[214:221], v[34:41], v[58:61], v209, v208 op_sel_hi:[0,0,0]
	v_mfma_scale_f32_16x16x128_f8f6f4 v[54:57], v[50:57], v[42:49], v[230:233], v209, v208 op_sel_hi:[0,0,0]
	v_mfma_scale_f32_16x16x128_f8f6f4 v[50:53], v[214:221], v[42:49], v[234:237], v209, v208 op_sel_hi:[0,0,0]
	s_setprio 0
	s_cmp_ge_i32 s59, s1
	s_barrier
	s_cbranch_scc1 .LBB0_1668
	s_mov_b64 s[22:23], s[24:25]
	s_branch .LBB0_1673
